# out-proj K-loops: first trip peeled too (C=0 on the first MFMA of each accumulator, incl. the one that changes registers), 128 zeroing v_mov per unit removed
# baseline (speedup 1.0000x reference)
;     __device__ __forceinline__ int brow(const pg8::Unit& u) const { return (u.pn >> 8) * Nper + (u.pn & 255) * 256; }
; template <class Epi, class Sched, bool ALIGN_EPI = false, bool SP2 = false, bool FP8 = false, bool GATHER = false>
; __device__ __forceinline__ void gemm_phase(PG8_LAS unsigned char* lds, const Gemm g, const Sched& S, const Epi& E) {
;     ...
;         const bool has_next = S.next(ui + 1, nxt);
;         const char* nA = (has_next && !GATHER) ? (const char*)g.A + (size_t)nxt.pm * tstep : cA; const char* nB = has_next ? (const char*)g.Bt + (size_t)S.brow(nxt) * (size_t)K * 2 : cB;
; #pragma nounroll
;         for (int t = 0; t < nt; t += 2) {
;             const bool last = (t == nt - 2);
;             const char* a1 = cA + (size_t)(t + 1) * kstep;
;             const char* a2 = last ? nA : cA + (size_t)(t + 2) * kstep; const char* b2 = last ? nB : cB + (size_t)(t + 2) * kstep;
;     ...
; #pragma unroll
;         for (int a = 0; a < 2; ++a)
; #pragma unroll
;             for (int b = 0; b < 2; ++b)
; #pragma unroll
;                 for (int m = 0; m < 4; ++m)
; #pragma unroll
;                     for (int n = 0; n < 2; ++n) acc[a][b][m][n] = (f32x4){0.f, 0.f, 0.f, 0.f};
;         cur = nxt; cA = nA; cB = nB; ++ui;
.LBB0_591:
	s_ashr_i32 s47, s46, 31
	s_lshl_b64 s[48:49], s[46:47], 19
	s_add_u32 s48, s65, s48
	s_addc_u32 s49, s66, s49
	s_and_b64 s[50:51], s[6:7], exec
	s_cselect_b32 s47, s49, s57
	s_cselect_b32 s85, s48, s56
	s_lshl_b32 s50, s84, 8
	s_ashr_i32 s51, s50, 31
	s_lshl_b64 s[50:51], s[50:51], 11
	s_add_u32 s50, s62, s50
	s_addc_u32 s51, s63, s51
	s_and_b64 s[60:61], s[6:7], exec
	s_cselect_b32 s86, s51, s59
	s_cselect_b32 s87, s50, s58
	s_lshl_b32 s54, s54, 8
	s_ashr_i32 s60, s52, 4
	s_ashr_i32 s55, s54, 31
	s_cmpk_lt_i32 s52, 0x100
	s_mul_i32 s88, s60, 0x1800
	s_mul_hi_i32 s60, s60, 0x1800
	s_cselect_b32 s61, s60, 0
	s_cselect_b32 s60, s88, 0x18000
	s_lshl_b64 s[60:61], s[60:61], 2
	s_add_u32 s88, s74, s60
	s_addc_u32 s89, s75, s61
	s_lshl_b64 s[60:61], s[54:55], 2
	s_add_u32 s60, s88, s60
	s_addc_u32 s61, s89, s61
	s_add_u32 s56, s56, 0x40080
	s_addc_u32 s57, s57, 0
	s_add_u32 s55, s58, 0x100
	v_lshl_add_u64 v[122:123], s[60:61], 0, v[162:163]
	s_addc_u32 s88, s59, 0
	s_mov_b32 s89, -2
	s_waitcnt vmcnt(0)

; #define PG8_STAGE(bufoff, gbase, voff) do { _Pragma("unroll") for (int _i = 0; _i < 2; ++_i) \
;         __builtin_amdgcn_global_load_lds((const unsigned*)((const char*)(gbase) + (voff)[_i]), (PG8_LAS unsigned*)(lds + (bufoff) + ldsw + _i * 8192), 16, 0, 0); } while (0)
; #define PG8_STAGE_A(bufoff, kbase, h, gv) do { if constexpr (GATHER) { PG8_STAGE(bufoff, kbase, (gv)[h]); } else { PG8_STAGE(bufoff, (kbase) + (h) * hstep, voffA); } } while (0)
; #define PG8_WAIT_V(n) asm volatile("s_waitcnt vmcnt(" #n ")" ::: "memory")
; #define PG8_WAIT_L(n) asm volatile("s_waitcnt lgkmcnt(" #n ")" ::: "memory")
; #define PG8_BAR __builtin_amdgcn_s_barrier()
; #define PG8_SCHED __builtin_amdgcn_sched_barrier(0)
; template <class Epi, class Sched, bool ALIGN_EPI = false, bool SP2 = false, bool FP8 = false, bool GATHER = false>
; __device__ __forceinline__ void gemm_phase(PG8_LAS unsigned char* lds, const Gemm g, const Sched& S, const Epi& E) {
;     ...
;             PG8_LDB(B0, 0, 0); PG8_LDB(B1, 0, 1); PG8_SCHED; PG8_LDA(At, 0, 0); PG8_STAGE_A(PG8_SA(1, 1), a1, 1, gcur);
;             PG8_WAIT_V(8); PG8_WAIT_L(0); PG8_BAR; PG8_MMA(0, 0, At, B0); PG8_MMA(0, 1, At, B1); PG8_BAR; PG8_SCHED;
;             PG8_LDA(At, 0, 1); PG8_STAGE(PG8_SB(0, 0), b2, voffB); PG8_STAGE(PG8_SB(0, 1), b2 + hstep, voffB); PG8_STAGE_A(PG8_SA(0, 0), a2, 0, gsel);
;             PG8_WAIT_V(8); PG8_WAIT_L(0); PG8_BAR; PG8_MMA(1, 0, At, B0); PG8_MMA(1, 1, At, B1); PG8_BAR; PG8_SCHED;
.Lpeel592_body:
	v_add_u32_e32 v136, s82, v169
	ds_read_b128 v[124:127], v136
	ds_read_b128 v[128:131], v136 offset:1024
	ds_read_b128 v[132:135], v136 offset:2048
	ds_read_b128 v[164:167], v136 offset:3072
	v_add_u32_e32 v136, s83, v169
	ds_read_b128 v[172:175], v136
	ds_read_b128 v[176:179], v136 offset:1024
	ds_read_b128 v[180:183], v136 offset:2048
	ds_read_b128 v[184:187], v136 offset:3072
	s_add_u32 s60, s56, 0xfffc0080
	s_addc_u32 s61, s57, -1
	s_and_b64 s[58:59], s[58:59], exec
	s_cselect_b32 s61, s61, s47
	s_cselect_b32 s60, s60, s85
	s_cselect_b32 s59, s88, s86
	s_cselect_b32 s58, s55, s87
	v_lshl_add_u64 v[136:137], s[56:57], 0, v[154:155]
	s_add_i32 m0, s53, 0xc000
	ds_read_b128 v[188:191], v170
	ds_read_b128 v[192:195], v170 offset:1024
	ds_read_b128 v[196:199], v170 offset:2048
	ds_read_b128 v[200:203], v170 offset:3072
	ds_read_b128 v[204:207], v170 offset:4096
	ds_read_b128 v[208:211], v170 offset:5120
	ds_read_b128 v[212:215], v170 offset:6144
	ds_read_b128 v[216:219], v170 offset:7168
	global_load_lds_dwordx4 v[136:137], off
	v_lshl_add_u64 v[136:137], s[56:57], 0, v[156:157]
	s_add_i32 m0, s53, 0xe000
	s_nop 0
	global_load_lds_dwordx4 v[136:137], off
	s_waitcnt vmcnt(8)
	s_waitcnt lgkmcnt(0)
	s_barrier
	s_setprio 1
	s_waitcnt lgkmcnt(0)
	v_mfma_f32_16x16x32_bf16 v[142:145], v[124:127], v[188:191], 0
	v_mfma_f32_16x16x32_bf16 v[136:139], v[132:135], v[188:191], 0
	v_mfma_f32_16x16x32_bf16 v[118:121], v[124:127], v[196:199], 0
	v_mfma_f32_16x16x32_bf16 v[106:109], v[132:135], v[196:199], 0
	v_mfma_f32_16x16x32_bf16 v[102:105], v[124:127], v[204:207], 0
	v_mfma_f32_16x16x32_bf16 v[90:93], v[132:135], v[204:207], 0
	v_mfma_f32_16x16x32_bf16 v[86:89], v[124:127], v[212:215], 0
	v_mfma_f32_16x16x32_bf16 v[74:77], v[132:135], v[212:215], 0
	v_mfma_f32_16x16x32_bf16 v[142:145], v[128:131], v[192:195], v[142:145]
	v_mfma_f32_16x16x32_bf16 v[136:139], v[164:167], v[192:195], v[136:139]
	v_mfma_f32_16x16x32_bf16 v[118:121], v[128:131], v[200:203], v[118:121]
	v_mfma_f32_16x16x32_bf16 v[106:109], v[164:167], v[200:203], v[106:109]
	v_mfma_f32_16x16x32_bf16 v[102:105], v[128:131], v[208:211], v[102:105]
	v_mfma_f32_16x16x32_bf16 v[90:93], v[164:167], v[208:211], v[90:93]
	v_mfma_f32_16x16x32_bf16 v[86:89], v[128:131], v[216:219], v[86:89]
	v_mfma_f32_16x16x32_bf16 v[74:77], v[164:167], v[216:219], v[74:77]
	s_setprio 0
	s_setprio 1
	v_mfma_f32_16x16x32_bf16 v[114:117], v[172:175], v[188:191], 0
	v_mfma_f32_16x16x32_bf16 v[110:113], v[180:183], v[188:191], 0
	v_mfma_f32_16x16x32_bf16 v[98:101], v[172:175], v[196:199], 0
	v_mfma_f32_16x16x32_bf16 v[94:97], v[180:183], v[196:199], 0
	v_mfma_f32_16x16x32_bf16 v[82:85], v[172:175], v[204:207], 0
	v_mfma_f32_16x16x32_bf16 v[78:81], v[180:183], v[204:207], 0
	v_mfma_f32_16x16x32_bf16 v[70:73], v[172:175], v[212:215], 0
	v_mfma_f32_16x16x32_bf16 v[66:69], v[180:183], v[212:215], 0
	v_mfma_f32_16x16x32_bf16 v[114:117], v[176:179], v[192:195], v[114:117]
	v_mfma_f32_16x16x32_bf16 v[110:113], v[184:187], v[192:195], v[110:113]
	v_mfma_f32_16x16x32_bf16 v[98:101], v[176:179], v[200:203], v[98:101]
	v_mfma_f32_16x16x32_bf16 v[94:97], v[184:187], v[200:203], v[94:97]
	v_mfma_f32_16x16x32_bf16 v[82:85], v[176:179], v[208:211], v[82:85]
	v_mfma_f32_16x16x32_bf16 v[78:81], v[184:187], v[208:211], v[78:81]
	v_mfma_f32_16x16x32_bf16 v[70:73], v[176:179], v[216:219], v[70:73]
	v_mfma_f32_16x16x32_bf16 v[66:69], v[184:187], v[216:219], v[66:69]
	s_setprio 0
	s_barrier
	s_add_i32 s90, s82, s67
	v_lshl_add_u64 v[220:221], s[58:59], 0, v[150:151]
	s_mov_b32 m0, s90
	ds_read_b128 v[188:191], v170 offset:16384
	ds_read_b128 v[192:195], v170 offset:17408
	ds_read_b128 v[196:199], v170 offset:18432
	ds_read_b128 v[200:203], v170 offset:19456
	ds_read_b128 v[204:207], v170 offset:20480
	ds_read_b128 v[208:211], v170 offset:21504
	ds_read_b128 v[212:215], v170 offset:22528
	ds_read_b128 v[216:219], v170 offset:23552
	global_load_lds_dwordx4 v[220:221], off
	s_add_i32 m0, s90, 0x2000
	s_add_u32 s90, s58, 0x40000
	v_lshl_add_u64 v[222:223], s[58:59], 0, v[146:147]
	s_addc_u32 s91, s59, 0
	s_add_i32 s92, s83, s67
	global_load_lds_dwordx4 v[222:223], off
	v_lshl_add_u64 v[140:141], s[90:91], 0, v[150:151]
	s_mov_b32 m0, s92
	v_lshl_add_u64 v[224:225], s[60:61], 0, v[152:153]
	global_load_lds_dwordx4 v[140:141], off
	v_lshl_add_u64 v[140:141], s[90:91], 0, v[146:147]
	s_add_i32 m0, s92, 0x2000
	v_lshl_add_u64 v[226:227], s[60:61], 0, v[148:149]
	global_load_lds_dwordx4 v[140:141], off
	s_mov_b32 m0, s53
	s_nop 0
	global_load_lds_dwordx4 v[224:225], off
	s_mov_b32 m0, s70
	s_nop 0
	global_load_lds_dwordx4 v[226:227], off
	s_waitcnt vmcnt(8)
	s_waitcnt lgkmcnt(0)
	s_barrier
; #define PG8_STAGE(bufoff, gbase, voff) do { _Pragma("unroll") for (int _i = 0; _i < 2; ++_i) \
;         __builtin_amdgcn_global_load_lds((const unsigned*)((const char*)(gbase) + (voff)[_i]), (PG8_LAS unsigned*)(lds + (bufoff) + ldsw + _i * 8192), 16, 0, 0); } while (0)
; #define PG8_STAGE_A(bufoff, kbase, h, gv) do { if constexpr (GATHER) { PG8_STAGE(bufoff, kbase, (gv)[h]); } else { PG8_STAGE(bufoff, (kbase) + (h) * hstep, voffA); } } while (0)
; #define PG8_WAIT_V(n) asm volatile("s_waitcnt vmcnt(" #n ")" ::: "memory")
; #define PG8_WAIT_L(n) asm volatile("s_waitcnt lgkmcnt(" #n ")" ::: "memory")
; #define PG8_BAR __builtin_amdgcn_s_barrier()
; #define PG8_SCHED __builtin_amdgcn_sched_barrier(0)
; template <class Epi, class Sched, bool ALIGN_EPI = false, bool SP2 = false, bool FP8 = false, bool GATHER = false>
; __device__ __forceinline__ void gemm_phase(PG8_LAS unsigned char* lds, const Gemm g, const Sched& S, const Epi& E) {
;     ...
;             PG8_WAIT_V(8); PG8_WAIT_L(0); PG8_BAR; PG8_MMA(1, 0, At, B0); PG8_MMA(1, 1, At, B1); PG8_BAR; PG8_SCHED;
;             PG8_LDB(B0, 1, 0); PG8_LDB(B1, 1, 1); PG8_SCHED; PG8_LDA(At, 1, 0); PG8_STAGE_A(PG8_SA(0, 1), a2, 1, gsel);
;             PG8_WAIT_V(8); PG8_WAIT_L(0); PG8_BAR; PG8_MMA(0, 0, At, B0); PG8_MMA(0, 1, At, B1); PG8_BAR; PG8_SCHED;
;             PG8_LDA(At, 1, 1); PG8_STAGE(PG8_SB(1, 0), b3, voffB); PG8_STAGE(PG8_SB(1, 1), b3 + hstep, voffB); PG8_STAGE_A(PG8_SA(1, 0), a3, 0, gsel);
	s_setprio 1
	s_waitcnt lgkmcnt(0)
	v_mfma_f32_16x16x32_bf16 v[62:65], v[124:127], v[188:191], 0
	v_mfma_f32_16x16x32_bf16 v[58:61], v[132:135], v[188:191], 0
	v_mfma_f32_16x16x32_bf16 v[54:57], v[124:127], v[196:199], 0
	v_mfma_f32_16x16x32_bf16 v[42:45], v[132:135], v[196:199], 0
	v_mfma_f32_16x16x32_bf16 v[38:41], v[124:127], v[204:207], 0
	v_mfma_f32_16x16x32_bf16 v[26:29], v[132:135], v[204:207], 0
	v_mfma_f32_16x16x32_bf16 v[22:25], v[124:127], v[212:215], 0
	v_mfma_f32_16x16x32_bf16 v[10:13], v[132:135], v[212:215], 0
	v_mfma_f32_16x16x32_bf16 v[62:65], v[128:131], v[192:195], v[62:65]
	v_mfma_f32_16x16x32_bf16 v[58:61], v[164:167], v[192:195], v[58:61]
	v_mfma_f32_16x16x32_bf16 v[54:57], v[128:131], v[200:203], v[54:57]
	v_mfma_f32_16x16x32_bf16 v[42:45], v[164:167], v[200:203], v[42:45]
	v_mfma_f32_16x16x32_bf16 v[38:41], v[128:131], v[208:211], v[38:41]
	v_mfma_f32_16x16x32_bf16 v[26:29], v[164:167], v[208:211], v[26:29]
	v_mfma_f32_16x16x32_bf16 v[22:25], v[128:131], v[216:219], v[22:25]
	v_mfma_f32_16x16x32_bf16 v[10:13], v[164:167], v[216:219], v[10:13]
	s_setprio 0
	s_setprio 1
	v_mfma_f32_16x16x32_bf16 v[50:53], v[172:175], v[188:191], 0
	v_mfma_f32_16x16x32_bf16 v[46:49], v[180:183], v[188:191], 0
	v_mfma_f32_16x16x32_bf16 v[34:37], v[172:175], v[196:199], 0
	v_mfma_f32_16x16x32_bf16 v[30:33], v[180:183], v[196:199], 0
	v_mfma_f32_16x16x32_bf16 v[18:21], v[172:175], v[204:207], 0
	v_mfma_f32_16x16x32_bf16 v[14:17], v[180:183], v[204:207], 0
	v_mfma_f32_16x16x32_bf16 v[6:9], v[172:175], v[212:215], 0
	v_mfma_f32_16x16x32_bf16 v[2:5], v[180:183], v[212:215], 0
	v_mfma_f32_16x16x32_bf16 v[50:53], v[176:179], v[192:195], v[50:53]
	v_mfma_f32_16x16x32_bf16 v[46:49], v[184:187], v[192:195], v[46:49]
	v_mfma_f32_16x16x32_bf16 v[34:37], v[176:179], v[200:203], v[34:37]
	v_mfma_f32_16x16x32_bf16 v[30:33], v[184:187], v[200:203], v[30:33]
	v_mfma_f32_16x16x32_bf16 v[18:21], v[176:179], v[208:211], v[18:21]
	v_mfma_f32_16x16x32_bf16 v[14:17], v[184:187], v[208:211], v[14:17]
	v_mfma_f32_16x16x32_bf16 v[6:9], v[176:179], v[216:219], v[6:9]
	v_mfma_f32_16x16x32_bf16 v[2:5], v[184:187], v[216:219], v[2:5]
	s_setprio 0
	s_barrier
	s_add_i32 s90, 0, 0x18000
	v_add_u32_e32 v140, s90, v169
	s_add_i32 s91, 0, 0x1c000
	ds_read_b128 v[124:127], v140
	ds_read_b128 v[128:131], v140 offset:1024
	ds_read_b128 v[132:135], v140 offset:2048
	ds_read_b128 v[164:167], v140 offset:3072
	v_add_u32_e32 v140, s91, v169
	ds_read_b128 v[172:175], v140
	ds_read_b128 v[176:179], v140 offset:1024
	ds_read_b128 v[180:183], v140 offset:2048
	ds_read_b128 v[184:187], v140 offset:3072
	s_add_u32 s60, s60, 0x40000
	s_addc_u32 s61, s61, 0
	s_mov_b32 m0, s71
	v_lshl_add_u64 v[140:141], s[60:61], 0, v[152:153]
	ds_read_b128 v[188:191], v170 offset:32768
	ds_read_b128 v[192:195], v170 offset:33792
	ds_read_b128 v[196:199], v170 offset:34816
	ds_read_b128 v[200:203], v170 offset:35840
	ds_read_b128 v[204:207], v170 offset:36864
	ds_read_b128 v[208:211], v170 offset:37888
	ds_read_b128 v[212:215], v170 offset:38912
	ds_read_b128 v[216:219], v170 offset:39936
	global_load_lds_dwordx4 v[140:141], off
	v_lshl_add_u64 v[140:141], s[60:61], 0, v[148:149]
	s_mov_b32 m0, s72
	s_nop 0
	global_load_lds_dwordx4 v[140:141], off
	s_waitcnt vmcnt(8)
	s_waitcnt lgkmcnt(0)
	s_barrier
	s_setprio 1
	s_waitcnt lgkmcnt(0)
	v_mfma_f32_16x16x32_bf16 v[140:143], v[124:127], v[188:191], v[142:145]
	v_mfma_f32_16x16x32_bf16 v[136:139], v[132:135], v[188:191], v[136:139]
	v_mfma_f32_16x16x32_bf16 v[118:121], v[124:127], v[196:199], v[118:121]
	v_mfma_f32_16x16x32_bf16 v[106:109], v[132:135], v[196:199], v[106:109]
	v_mfma_f32_16x16x32_bf16 v[102:105], v[124:127], v[204:207], v[102:105]
	v_mfma_f32_16x16x32_bf16 v[90:93], v[132:135], v[204:207], v[90:93]
	v_mfma_f32_16x16x32_bf16 v[86:89], v[124:127], v[212:215], v[86:89]
	v_mfma_f32_16x16x32_bf16 v[74:77], v[132:135], v[212:215], v[74:77]
	v_mfma_f32_16x16x32_bf16 v[142:145], v[128:131], v[192:195], v[140:143]
	v_mfma_f32_16x16x32_bf16 v[138:141], v[164:167], v[192:195], v[136:139]
	v_mfma_f32_16x16x32_bf16 v[118:121], v[128:131], v[200:203], v[118:121]
	v_mfma_f32_16x16x32_bf16 v[106:109], v[164:167], v[200:203], v[106:109]
	v_mfma_f32_16x16x32_bf16 v[102:105], v[128:131], v[208:211], v[102:105]
	v_mfma_f32_16x16x32_bf16 v[90:93], v[164:167], v[208:211], v[90:93]
	v_mfma_f32_16x16x32_bf16 v[86:89], v[128:131], v[216:219], v[86:89]
	v_mfma_f32_16x16x32_bf16 v[74:77], v[164:167], v[216:219], v[74:77]
	s_setprio 0
	s_setprio 1
	v_mfma_f32_16x16x32_bf16 v[114:117], v[172:175], v[188:191], v[114:117]
	v_mfma_f32_16x16x32_bf16 v[110:113], v[180:183], v[188:191], v[110:113]
	v_mfma_f32_16x16x32_bf16 v[98:101], v[172:175], v[196:199], v[98:101]
	v_mfma_f32_16x16x32_bf16 v[94:97], v[180:183], v[196:199], v[94:97]
	v_mfma_f32_16x16x32_bf16 v[82:85], v[172:175], v[204:207], v[82:85]
	v_mfma_f32_16x16x32_bf16 v[78:81], v[180:183], v[204:207], v[78:81]
	v_mfma_f32_16x16x32_bf16 v[70:73], v[172:175], v[212:215], v[70:73]
	v_mfma_f32_16x16x32_bf16 v[66:69], v[180:183], v[212:215], v[66:69]
	v_mfma_f32_16x16x32_bf16 v[114:117], v[176:179], v[192:195], v[114:117]
	v_mfma_f32_16x16x32_bf16 v[110:113], v[184:187], v[192:195], v[110:113]
	v_mfma_f32_16x16x32_bf16 v[98:101], v[176:179], v[200:203], v[98:101]
	v_mfma_f32_16x16x32_bf16 v[94:97], v[184:187], v[200:203], v[94:97]
	v_mfma_f32_16x16x32_bf16 v[82:85], v[176:179], v[208:211], v[82:85]
	v_mfma_f32_16x16x32_bf16 v[78:81], v[184:187], v[208:211], v[78:81]
	v_mfma_f32_16x16x32_bf16 v[70:73], v[176:179], v[216:219], v[70:73]
	v_mfma_f32_16x16x32_bf16 v[66:69], v[184:187], v[216:219], v[66:69]
	s_setprio 0
	s_barrier
; #define PG8_STAGE(bufoff, gbase, voff) do { _Pragma("unroll") for (int _i = 0; _i < 2; ++_i) \
;         __builtin_amdgcn_global_load_lds((const unsigned*)((const char*)(gbase) + (voff)[_i]), (PG8_LAS unsigned*)(lds + (bufoff) + ldsw + _i * 8192), 16, 0, 0); } while (0)
; #define PG8_STAGE_A(bufoff, kbase, h, gv) do { if constexpr (GATHER) { PG8_STAGE(bufoff, kbase, (gv)[h]); } else { PG8_STAGE(bufoff, (kbase) + (h) * hstep, voffA); } } while (0)
; #define PG8_WAIT_V(n) asm volatile("s_waitcnt vmcnt(" #n ")" ::: "memory")
; #define PG8_WAIT_L(n) asm volatile("s_waitcnt lgkmcnt(" #n ")" ::: "memory")
; #define PG8_BAR __builtin_amdgcn_s_barrier()
; #define PG8_SCHED __builtin_amdgcn_sched_barrier(0)
; template <class Epi, class Sched, bool ALIGN_EPI = false, bool SP2 = false, bool FP8 = false, bool GATHER = false>
; __device__ __forceinline__ void gemm_phase(PG8_LAS unsigned char* lds, const Gemm g, const Sched& S, const Epi& E) {
;     ...
;         for (int t = 0; t < nt; t += 2) {
;             const bool last = (t == nt - 2);
;             const char* a1 = cA + (size_t)(t + 1) * kstep;
;             const char* a2 = last ? nA : cA + (size_t)(t + 2) * kstep; const char* b2 = last ? nB : cB + (size_t)(t + 2) * kstep;
;     ...
;             PG8_LDA(At, 1, 1); PG8_STAGE(PG8_SB(1, 0), b3, voffB); PG8_STAGE(PG8_SB(1, 1), b3 + hstep, voffB); PG8_STAGE_A(PG8_SA(1, 0), a3, 0, gsel);
;             PG8_WAIT_V(8); PG8_WAIT_L(0); PG8_BAR; PG8_MMA(1, 0, At, B0); PG8_MMA(1, 1, At, B1); PG8_BAR; PG8_SCHED;
	s_add_i32 s60, s90, s67
	v_lshl_add_u64 v[136:137], v[220:221], 0, s[18:19]
	s_mov_b32 m0, s60
	ds_read_b128 v[188:191], v170 offset:49152
	ds_read_b128 v[192:195], v170 offset:50176
	ds_read_b128 v[196:199], v170 offset:51200
	ds_read_b128 v[200:203], v170 offset:52224
	ds_read_b128 v[204:207], v170 offset:53248
	ds_read_b128 v[208:211], v170 offset:54272
	ds_read_b128 v[212:215], v170 offset:55296
	ds_read_b128 v[216:219], v170 offset:56320
	global_load_lds_dwordx4 v[136:137], off
	s_add_i32 m0, s60, 0x2000
	s_add_u32 s58, s58, 0x40080
	v_lshl_add_u64 v[136:137], v[222:223], 0, s[18:19]
	s_addc_u32 s59, s59, 0
	s_add_i32 s60, s91, s67
	global_load_lds_dwordx4 v[136:137], off
	v_lshl_add_u64 v[136:137], s[58:59], 0, v[150:151]
	s_mov_b32 m0, s60
	s_nop 0
	global_load_lds_dwordx4 v[136:137], off
	v_lshl_add_u64 v[136:137], s[58:59], 0, v[146:147]
	s_add_i32 m0, s60, 0x2000
	s_nop 0
	global_load_lds_dwordx4 v[136:137], off
	v_lshl_add_u64 v[136:137], v[224:225], 0, s[18:19]
	s_mov_b32 m0, s78
	s_nop 0
	global_load_lds_dwordx4 v[136:137], off
	v_lshl_add_u64 v[136:137], v[226:227], 0, s[18:19]
	s_mov_b32 m0, s79
	s_nop 0
	global_load_lds_dwordx4 v[136:137], off
	s_waitcnt vmcnt(8)
	s_waitcnt lgkmcnt(0)
	s_barrier
	s_setprio 1
	s_waitcnt lgkmcnt(0)
	v_mfma_f32_16x16x32_bf16 v[62:65], v[124:127], v[188:191], v[62:65]
	v_mfma_f32_16x16x32_bf16 v[58:61], v[132:135], v[188:191], v[58:61]
	v_mfma_f32_16x16x32_bf16 v[54:57], v[124:127], v[196:199], v[54:57]
	v_mfma_f32_16x16x32_bf16 v[42:45], v[132:135], v[196:199], v[42:45]
	v_mfma_f32_16x16x32_bf16 v[38:41], v[124:127], v[204:207], v[38:41]
	v_mfma_f32_16x16x32_bf16 v[26:29], v[132:135], v[204:207], v[26:29]
	v_mfma_f32_16x16x32_bf16 v[22:25], v[124:127], v[212:215], v[22:25]
	v_mfma_f32_16x16x32_bf16 v[10:13], v[132:135], v[212:215], v[10:13]
	v_mfma_f32_16x16x32_bf16 v[62:65], v[128:131], v[192:195], v[62:65]
	v_mfma_f32_16x16x32_bf16 v[58:61], v[164:167], v[192:195], v[58:61]
	v_mfma_f32_16x16x32_bf16 v[54:57], v[128:131], v[200:203], v[54:57]
	v_mfma_f32_16x16x32_bf16 v[42:45], v[164:167], v[200:203], v[42:45]
	v_mfma_f32_16x16x32_bf16 v[38:41], v[128:131], v[208:211], v[38:41]
	v_mfma_f32_16x16x32_bf16 v[26:29], v[164:167], v[208:211], v[26:29]
	v_mfma_f32_16x16x32_bf16 v[22:25], v[128:131], v[216:219], v[22:25]
	v_mfma_f32_16x16x32_bf16 v[10:13], v[164:167], v[216:219], v[10:13]
	s_setprio 0
	s_setprio 1
	v_mfma_f32_16x16x32_bf16 v[50:53], v[172:175], v[188:191], v[50:53]
	v_mfma_f32_16x16x32_bf16 v[46:49], v[180:183], v[188:191], v[46:49]
	v_mfma_f32_16x16x32_bf16 v[34:37], v[172:175], v[196:199], v[34:37]
	v_mfma_f32_16x16x32_bf16 v[30:33], v[180:183], v[196:199], v[30:33]
	v_mfma_f32_16x16x32_bf16 v[18:21], v[172:175], v[204:207], v[18:21]
	v_mfma_f32_16x16x32_bf16 v[14:17], v[180:183], v[204:207], v[14:17]
	v_mfma_f32_16x16x32_bf16 v[6:9], v[172:175], v[212:215], v[6:9]
	v_mfma_f32_16x16x32_bf16 v[2:5], v[180:183], v[212:215], v[2:5]
	v_mfma_f32_16x16x32_bf16 v[50:53], v[176:179], v[192:195], v[50:53]
	v_mfma_f32_16x16x32_bf16 v[46:49], v[184:187], v[192:195], v[46:49]
	v_mfma_f32_16x16x32_bf16 v[34:37], v[176:179], v[200:203], v[34:37]
	v_mfma_f32_16x16x32_bf16 v[30:33], v[184:187], v[200:203], v[30:33]
	v_mfma_f32_16x16x32_bf16 v[18:21], v[176:179], v[208:211], v[18:21]
	v_mfma_f32_16x16x32_bf16 v[14:17], v[184:187], v[208:211], v[14:17]
	v_mfma_f32_16x16x32_bf16 v[6:9], v[176:179], v[216:219], v[6:9]
	v_mfma_f32_16x16x32_bf16 v[2:5], v[184:187], v[216:219], v[2:5]
	s_setprio 0
	s_add_i32 s89, s89, 2
	s_add_u32 s56, s56, 0x100
	s_addc_u32 s57, s57, 0
	s_add_u32 s55, s55, 0x100
	s_addc_u32 s88, s88, 0
	s_cmp_gt_u32 s89, 13
	s_cbranch_scc1 .Lrot592_exit
	s_barrier
	s_branch .LBB0_593

;     __device__ __forceinline__ int brow(const pg8::Unit& u) const { return (u.pn >> 8) * Nper + (u.pn & 255) * 256; }
; template <class Epi, class Sched, bool ALIGN_EPI = false, bool SP2 = false, bool FP8 = false, bool GATHER = false>
; __device__ __forceinline__ void gemm_phase(PG8_LAS unsigned char* lds, const Gemm g, const Sched& S, const Epi& E) {
;     ...
;         const bool has_next = S.next(ui + 1, nxt);
;         const char* nA = (has_next && !GATHER) ? (const char*)g.A + (size_t)nxt.pm * tstep : cA; const char* nB = has_next ? (const char*)g.Bt + (size_t)S.brow(nxt) * (size_t)K * 2 : cB;
; #pragma nounroll
;         for (int t = 0; t < nt; t += 2) {
;             const bool last = (t == nt - 2);
;             const char* a1 = cA + (size_t)(t + 1) * kstep;
;             const char* a2 = last ? nA : cA + (size_t)(t + 2) * kstep; const char* b2 = last ? nB : cB + (size_t)(t + 2) * kstep;
;     ...
; #pragma unroll
;         for (int a = 0; a < 2; ++a)
; #pragma unroll
;             for (int b = 0; b < 2; ++b)
; #pragma unroll
;                 for (int m = 0; m < 4; ++m)
; #pragma unroll
;                     for (int n = 0; n < 2; ++n) acc[a][b][m][n] = (f32x4){0.f, 0.f, 0.f, 0.f};
;         cur = nxt; cA = nA; cB = nB; ++ui;
.LBB0_1496:
	s_ashr_i32 s45, s44, 31
	s_lshl_b64 s[46:47], s[44:45], 19
	s_add_u32 s46, s61, s46
	s_addc_u32 s47, s62, s47
	s_and_b64 s[48:49], s[4:5], exec
	s_cselect_b32 s45, s47, s55
	s_cselect_b32 s82, s46, s54
	s_lshl_b32 s48, s81, 8
	s_ashr_i32 s49, s48, 31
	s_lshl_b64 s[48:49], s[48:49], 11
	s_add_u32 s48, s63, s48
	s_addc_u32 s49, s65, s49
	s_and_b64 s[58:59], s[4:5], exec
	s_cselect_b32 s83, s49, s57
	s_cselect_b32 s84, s48, s56
	s_lshl_b32 s52, s52, 8
	s_ashr_i32 s58, s50, 4
	s_ashr_i32 s53, s52, 31
	s_cmpk_lt_i32 s50, 0x100
	s_mul_i32 s85, s58, 0x1800
	s_mul_hi_i32 s58, s58, 0x1800
	s_cselect_b32 s59, s58, 0
	s_cselect_b32 s58, s85, 0x18000
	s_lshl_b64 s[58:59], s[58:59], 2
	s_add_u32 s85, s71, s58
	s_addc_u32 s86, s72, s59
	s_lshl_b64 s[58:59], s[52:53], 2
	s_add_u32 s58, s85, s58
	s_addc_u32 s59, s86, s59
	s_add_u32 s54, s54, 0x40080
	s_addc_u32 s55, s55, 0
	s_add_u32 s53, s56, 0x100
	v_lshl_add_u64 v[122:123], s[58:59], 0, v[162:163]
	s_addc_u32 s85, s57, 0
	s_mov_b32 s86, -2
	s_waitcnt vmcnt(0)

; #define PG8_STAGE(bufoff, gbase, voff) do { _Pragma("unroll") for (int _i = 0; _i < 2; ++_i) \
;         __builtin_amdgcn_global_load_lds((const unsigned*)((const char*)(gbase) + (voff)[_i]), (PG8_LAS unsigned*)(lds + (bufoff) + ldsw + _i * 8192), 16, 0, 0); } while (0)
; #define PG8_STAGE_A(bufoff, kbase, h, gv) do { if constexpr (GATHER) { PG8_STAGE(bufoff, kbase, (gv)[h]); } else { PG8_STAGE(bufoff, (kbase) + (h) * hstep, voffA); } } while (0)
; #define PG8_WAIT_V(n) asm volatile("s_waitcnt vmcnt(" #n ")" ::: "memory")
; #define PG8_WAIT_L(n) asm volatile("s_waitcnt lgkmcnt(" #n ")" ::: "memory")
; #define PG8_BAR __builtin_amdgcn_s_barrier()
; #define PG8_SCHED __builtin_amdgcn_sched_barrier(0)
; template <class Epi, class Sched, bool ALIGN_EPI = false, bool SP2 = false, bool FP8 = false, bool GATHER = false>
; __device__ __forceinline__ void gemm_phase(PG8_LAS unsigned char* lds, const Gemm g, const Sched& S, const Epi& E) {
;     ...
;             PG8_LDB(B0, 0, 0); PG8_LDB(B1, 0, 1); PG8_SCHED; PG8_LDA(At, 0, 0); PG8_STAGE_A(PG8_SA(1, 1), a1, 1, gcur);
;             PG8_WAIT_V(8); PG8_WAIT_L(0); PG8_BAR; PG8_MMA(0, 0, At, B0); PG8_MMA(0, 1, At, B1); PG8_BAR; PG8_SCHED;
;             PG8_LDA(At, 0, 1); PG8_STAGE(PG8_SB(0, 0), b2, voffB); PG8_STAGE(PG8_SB(0, 1), b2 + hstep, voffB); PG8_STAGE_A(PG8_SA(0, 0), a2, 0, gsel);
;             PG8_WAIT_V(8); PG8_WAIT_L(0); PG8_BAR; PG8_MMA(1, 0, At, B0); PG8_MMA(1, 1, At, B1); PG8_BAR; PG8_SCHED;
.Lpeel1497_body:
	v_add_u32_e32 v136, s79, v169
	ds_read_b128 v[124:127], v136
	ds_read_b128 v[128:131], v136 offset:1024
	ds_read_b128 v[132:135], v136 offset:2048
	ds_read_b128 v[164:167], v136 offset:3072
	v_add_u32_e32 v136, s80, v169
	ds_read_b128 v[172:175], v136
	ds_read_b128 v[176:179], v136 offset:1024
	ds_read_b128 v[180:183], v136 offset:2048
	ds_read_b128 v[184:187], v136 offset:3072
	s_add_u32 s58, s54, 0xfffc0080
	s_addc_u32 s59, s55, -1
	s_and_b64 s[56:57], s[56:57], exec
	s_cselect_b32 s59, s59, s45
	s_cselect_b32 s58, s58, s82
	s_cselect_b32 s57, s85, s83
	s_cselect_b32 s56, s53, s84
	v_lshl_add_u64 v[136:137], s[54:55], 0, v[154:155]
	s_add_i32 m0, s51, 0xc000
	ds_read_b128 v[188:191], v170
	ds_read_b128 v[192:195], v170 offset:1024
	ds_read_b128 v[196:199], v170 offset:2048
	ds_read_b128 v[200:203], v170 offset:3072
	ds_read_b128 v[204:207], v170 offset:4096
	ds_read_b128 v[208:211], v170 offset:5120
	ds_read_b128 v[212:215], v170 offset:6144
	ds_read_b128 v[216:219], v170 offset:7168
	global_load_lds_dwordx4 v[136:137], off
	v_lshl_add_u64 v[136:137], s[54:55], 0, v[156:157]
	s_add_i32 m0, s51, 0xe000
	s_nop 0
	global_load_lds_dwordx4 v[136:137], off
	s_waitcnt vmcnt(8)
	s_waitcnt lgkmcnt(0)
	s_barrier
	s_setprio 1
	s_waitcnt lgkmcnt(0)
	v_mfma_f32_16x16x32_bf16 v[142:145], v[124:127], v[188:191], 0
	v_mfma_f32_16x16x32_bf16 v[136:139], v[132:135], v[188:191], 0
	v_mfma_f32_16x16x32_bf16 v[118:121], v[124:127], v[196:199], 0
	v_mfma_f32_16x16x32_bf16 v[106:109], v[132:135], v[196:199], 0
	v_mfma_f32_16x16x32_bf16 v[102:105], v[124:127], v[204:207], 0
	v_mfma_f32_16x16x32_bf16 v[90:93], v[132:135], v[204:207], 0
	v_mfma_f32_16x16x32_bf16 v[86:89], v[124:127], v[212:215], 0
	v_mfma_f32_16x16x32_bf16 v[74:77], v[132:135], v[212:215], 0
	v_mfma_f32_16x16x32_bf16 v[142:145], v[128:131], v[192:195], v[142:145]
	v_mfma_f32_16x16x32_bf16 v[136:139], v[164:167], v[192:195], v[136:139]
	v_mfma_f32_16x16x32_bf16 v[118:121], v[128:131], v[200:203], v[118:121]
	v_mfma_f32_16x16x32_bf16 v[106:109], v[164:167], v[200:203], v[106:109]
	v_mfma_f32_16x16x32_bf16 v[102:105], v[128:131], v[208:211], v[102:105]
	v_mfma_f32_16x16x32_bf16 v[90:93], v[164:167], v[208:211], v[90:93]
	v_mfma_f32_16x16x32_bf16 v[86:89], v[128:131], v[216:219], v[86:89]
	v_mfma_f32_16x16x32_bf16 v[74:77], v[164:167], v[216:219], v[74:77]
	s_setprio 0
	s_setprio 1
	v_mfma_f32_16x16x32_bf16 v[114:117], v[172:175], v[188:191], 0
	v_mfma_f32_16x16x32_bf16 v[110:113], v[180:183], v[188:191], 0
	v_mfma_f32_16x16x32_bf16 v[98:101], v[172:175], v[196:199], 0
	v_mfma_f32_16x16x32_bf16 v[94:97], v[180:183], v[196:199], 0
	v_mfma_f32_16x16x32_bf16 v[82:85], v[172:175], v[204:207], 0
	v_mfma_f32_16x16x32_bf16 v[78:81], v[180:183], v[204:207], 0
	v_mfma_f32_16x16x32_bf16 v[70:73], v[172:175], v[212:215], 0
	v_mfma_f32_16x16x32_bf16 v[66:69], v[180:183], v[212:215], 0
	v_mfma_f32_16x16x32_bf16 v[114:117], v[176:179], v[192:195], v[114:117]
	v_mfma_f32_16x16x32_bf16 v[110:113], v[184:187], v[192:195], v[110:113]
	v_mfma_f32_16x16x32_bf16 v[98:101], v[176:179], v[200:203], v[98:101]
	v_mfma_f32_16x16x32_bf16 v[94:97], v[184:187], v[200:203], v[94:97]
	v_mfma_f32_16x16x32_bf16 v[82:85], v[176:179], v[208:211], v[82:85]
	v_mfma_f32_16x16x32_bf16 v[78:81], v[184:187], v[208:211], v[78:81]
	v_mfma_f32_16x16x32_bf16 v[70:73], v[176:179], v[216:219], v[70:73]
	v_mfma_f32_16x16x32_bf16 v[66:69], v[184:187], v[216:219], v[66:69]
	s_setprio 0
	s_barrier
	s_add_i32 s87, s79, s66
	v_lshl_add_u64 v[220:221], s[56:57], 0, v[148:149]
	s_mov_b32 m0, s87
	ds_read_b128 v[188:191], v170 offset:16384
	ds_read_b128 v[192:195], v170 offset:17408
	ds_read_b128 v[196:199], v170 offset:18432
	ds_read_b128 v[200:203], v170 offset:19456
	ds_read_b128 v[204:207], v170 offset:20480
	ds_read_b128 v[208:211], v170 offset:21504
	ds_read_b128 v[212:215], v170 offset:22528
	ds_read_b128 v[216:219], v170 offset:23552
	global_load_lds_dwordx4 v[220:221], off
	s_add_i32 m0, s87, 0x2000
	s_add_u32 s88, s56, 0x40000
	v_lshl_add_u64 v[222:223], s[56:57], 0, v[152:153]
	s_addc_u32 s89, s57, 0
	s_add_i32 s87, s80, s66
	global_load_lds_dwordx4 v[222:223], off
	v_lshl_add_u64 v[140:141], s[88:89], 0, v[148:149]
	s_mov_b32 m0, s87
	v_lshl_add_u64 v[224:225], s[58:59], 0, v[146:147]
	global_load_lds_dwordx4 v[140:141], off
	v_lshl_add_u64 v[140:141], s[88:89], 0, v[152:153]
	s_add_i32 m0, s87, 0x2000
	v_lshl_add_u64 v[226:227], s[58:59], 0, v[150:151]
	global_load_lds_dwordx4 v[140:141], off
	s_mov_b32 m0, s51
	s_nop 0
	global_load_lds_dwordx4 v[224:225], off
	s_mov_b32 m0, s67
	s_nop 0
	global_load_lds_dwordx4 v[226:227], off
	s_waitcnt vmcnt(8)
	s_waitcnt lgkmcnt(0)
	s_barrier
; #define PG8_STAGE(bufoff, gbase, voff) do { _Pragma("unroll") for (int _i = 0; _i < 2; ++_i) \
;         __builtin_amdgcn_global_load_lds((const unsigned*)((const char*)(gbase) + (voff)[_i]), (PG8_LAS unsigned*)(lds + (bufoff) + ldsw + _i * 8192), 16, 0, 0); } while (0)
; #define PG8_STAGE_A(bufoff, kbase, h, gv) do { if constexpr (GATHER) { PG8_STAGE(bufoff, kbase, (gv)[h]); } else { PG8_STAGE(bufoff, (kbase) + (h) * hstep, voffA); } } while (0)
; #define PG8_WAIT_V(n) asm volatile("s_waitcnt vmcnt(" #n ")" ::: "memory")
; #define PG8_WAIT_L(n) asm volatile("s_waitcnt lgkmcnt(" #n ")" ::: "memory")
; #define PG8_BAR __builtin_amdgcn_s_barrier()
; #define PG8_SCHED __builtin_amdgcn_sched_barrier(0)
; template <class Epi, class Sched, bool ALIGN_EPI = false, bool SP2 = false, bool FP8 = false, bool GATHER = false>
; __device__ __forceinline__ void gemm_phase(PG8_LAS unsigned char* lds, const Gemm g, const Sched& S, const Epi& E) {
;     ...
;             PG8_WAIT_V(8); PG8_WAIT_L(0); PG8_BAR; PG8_MMA(1, 0, At, B0); PG8_MMA(1, 1, At, B1); PG8_BAR; PG8_SCHED;
;             PG8_LDB(B0, 1, 0); PG8_LDB(B1, 1, 1); PG8_SCHED; PG8_LDA(At, 1, 0); PG8_STAGE_A(PG8_SA(0, 1), a2, 1, gsel);
;             PG8_WAIT_V(8); PG8_WAIT_L(0); PG8_BAR; PG8_MMA(0, 0, At, B0); PG8_MMA(0, 1, At, B1); PG8_BAR; PG8_SCHED;
;             PG8_LDA(At, 1, 1); PG8_STAGE(PG8_SB(1, 0), b3, voffB); PG8_STAGE(PG8_SB(1, 1), b3 + hstep, voffB); PG8_STAGE_A(PG8_SA(1, 0), a3, 0, gsel);
	s_setprio 1
	s_waitcnt lgkmcnt(0)
	v_mfma_f32_16x16x32_bf16 v[62:65], v[124:127], v[188:191], 0
	v_mfma_f32_16x16x32_bf16 v[58:61], v[132:135], v[188:191], 0
	v_mfma_f32_16x16x32_bf16 v[54:57], v[124:127], v[196:199], 0
	v_mfma_f32_16x16x32_bf16 v[42:45], v[132:135], v[196:199], 0
	v_mfma_f32_16x16x32_bf16 v[38:41], v[124:127], v[204:207], 0
	v_mfma_f32_16x16x32_bf16 v[26:29], v[132:135], v[204:207], 0
	v_mfma_f32_16x16x32_bf16 v[22:25], v[124:127], v[212:215], 0
	v_mfma_f32_16x16x32_bf16 v[10:13], v[132:135], v[212:215], 0
	v_mfma_f32_16x16x32_bf16 v[62:65], v[128:131], v[192:195], v[62:65]
	v_mfma_f32_16x16x32_bf16 v[58:61], v[164:167], v[192:195], v[58:61]
	v_mfma_f32_16x16x32_bf16 v[54:57], v[128:131], v[200:203], v[54:57]
	v_mfma_f32_16x16x32_bf16 v[42:45], v[164:167], v[200:203], v[42:45]
	v_mfma_f32_16x16x32_bf16 v[38:41], v[128:131], v[208:211], v[38:41]
	v_mfma_f32_16x16x32_bf16 v[26:29], v[164:167], v[208:211], v[26:29]
	v_mfma_f32_16x16x32_bf16 v[22:25], v[128:131], v[216:219], v[22:25]
	v_mfma_f32_16x16x32_bf16 v[10:13], v[164:167], v[216:219], v[10:13]
	s_setprio 0
	s_setprio 1
	v_mfma_f32_16x16x32_bf16 v[50:53], v[172:175], v[188:191], 0
	v_mfma_f32_16x16x32_bf16 v[46:49], v[180:183], v[188:191], 0
	v_mfma_f32_16x16x32_bf16 v[34:37], v[172:175], v[196:199], 0
	v_mfma_f32_16x16x32_bf16 v[30:33], v[180:183], v[196:199], 0
	v_mfma_f32_16x16x32_bf16 v[18:21], v[172:175], v[204:207], 0
	v_mfma_f32_16x16x32_bf16 v[14:17], v[180:183], v[204:207], 0
	v_mfma_f32_16x16x32_bf16 v[6:9], v[172:175], v[212:215], 0
	v_mfma_f32_16x16x32_bf16 v[2:5], v[180:183], v[212:215], 0
	v_mfma_f32_16x16x32_bf16 v[50:53], v[176:179], v[192:195], v[50:53]
	v_mfma_f32_16x16x32_bf16 v[46:49], v[184:187], v[192:195], v[46:49]
	v_mfma_f32_16x16x32_bf16 v[34:37], v[176:179], v[200:203], v[34:37]
	v_mfma_f32_16x16x32_bf16 v[30:33], v[184:187], v[200:203], v[30:33]
	v_mfma_f32_16x16x32_bf16 v[18:21], v[176:179], v[208:211], v[18:21]
	v_mfma_f32_16x16x32_bf16 v[14:17], v[184:187], v[208:211], v[14:17]
	v_mfma_f32_16x16x32_bf16 v[6:9], v[176:179], v[216:219], v[6:9]
	v_mfma_f32_16x16x32_bf16 v[2:5], v[184:187], v[216:219], v[2:5]
	s_setprio 0
	s_barrier
	s_add_i32 s87, 0, 0x18000
	v_add_u32_e32 v140, s87, v169
	s_add_i32 s88, 0, 0x1c000
	ds_read_b128 v[124:127], v140
	ds_read_b128 v[128:131], v140 offset:1024
	ds_read_b128 v[132:135], v140 offset:2048
	ds_read_b128 v[164:167], v140 offset:3072
	v_add_u32_e32 v140, s88, v169
	ds_read_b128 v[172:175], v140
	ds_read_b128 v[176:179], v140 offset:1024
	ds_read_b128 v[180:183], v140 offset:2048
	ds_read_b128 v[184:187], v140 offset:3072
	s_add_u32 s58, s58, 0x40000
	s_addc_u32 s59, s59, 0
	s_mov_b32 m0, s68
	v_lshl_add_u64 v[140:141], s[58:59], 0, v[146:147]
	ds_read_b128 v[188:191], v170 offset:32768
	ds_read_b128 v[192:195], v170 offset:33792
	ds_read_b128 v[196:199], v170 offset:34816
	ds_read_b128 v[200:203], v170 offset:35840
	ds_read_b128 v[204:207], v170 offset:36864
	ds_read_b128 v[208:211], v170 offset:37888
	ds_read_b128 v[212:215], v170 offset:38912
	ds_read_b128 v[216:219], v170 offset:39936
	global_load_lds_dwordx4 v[140:141], off
	v_lshl_add_u64 v[140:141], s[58:59], 0, v[150:151]
	s_mov_b32 m0, s69
	s_nop 0
	global_load_lds_dwordx4 v[140:141], off
	s_waitcnt vmcnt(8)
	s_waitcnt lgkmcnt(0)
	s_barrier
	s_setprio 1
	s_waitcnt lgkmcnt(0)
	v_mfma_f32_16x16x32_bf16 v[140:143], v[124:127], v[188:191], v[142:145]
	v_mfma_f32_16x16x32_bf16 v[136:139], v[132:135], v[188:191], v[136:139]
	v_mfma_f32_16x16x32_bf16 v[118:121], v[124:127], v[196:199], v[118:121]
	v_mfma_f32_16x16x32_bf16 v[106:109], v[132:135], v[196:199], v[106:109]
	v_mfma_f32_16x16x32_bf16 v[102:105], v[124:127], v[204:207], v[102:105]
	v_mfma_f32_16x16x32_bf16 v[90:93], v[132:135], v[204:207], v[90:93]
	v_mfma_f32_16x16x32_bf16 v[86:89], v[124:127], v[212:215], v[86:89]
	v_mfma_f32_16x16x32_bf16 v[74:77], v[132:135], v[212:215], v[74:77]
	v_mfma_f32_16x16x32_bf16 v[142:145], v[128:131], v[192:195], v[140:143]
	v_mfma_f32_16x16x32_bf16 v[138:141], v[164:167], v[192:195], v[136:139]
	v_mfma_f32_16x16x32_bf16 v[118:121], v[128:131], v[200:203], v[118:121]
	v_mfma_f32_16x16x32_bf16 v[106:109], v[164:167], v[200:203], v[106:109]
	v_mfma_f32_16x16x32_bf16 v[102:105], v[128:131], v[208:211], v[102:105]
	v_mfma_f32_16x16x32_bf16 v[90:93], v[164:167], v[208:211], v[90:93]
	v_mfma_f32_16x16x32_bf16 v[86:89], v[128:131], v[216:219], v[86:89]
	v_mfma_f32_16x16x32_bf16 v[74:77], v[164:167], v[216:219], v[74:77]
	s_setprio 0
	s_setprio 1
	v_mfma_f32_16x16x32_bf16 v[114:117], v[172:175], v[188:191], v[114:117]
	v_mfma_f32_16x16x32_bf16 v[110:113], v[180:183], v[188:191], v[110:113]
	v_mfma_f32_16x16x32_bf16 v[98:101], v[172:175], v[196:199], v[98:101]
	v_mfma_f32_16x16x32_bf16 v[94:97], v[180:183], v[196:199], v[94:97]
	v_mfma_f32_16x16x32_bf16 v[82:85], v[172:175], v[204:207], v[82:85]
	v_mfma_f32_16x16x32_bf16 v[78:81], v[180:183], v[204:207], v[78:81]
	v_mfma_f32_16x16x32_bf16 v[70:73], v[172:175], v[212:215], v[70:73]
	v_mfma_f32_16x16x32_bf16 v[66:69], v[180:183], v[212:215], v[66:69]
	v_mfma_f32_16x16x32_bf16 v[114:117], v[176:179], v[192:195], v[114:117]
	v_mfma_f32_16x16x32_bf16 v[110:113], v[184:187], v[192:195], v[110:113]
	v_mfma_f32_16x16x32_bf16 v[98:101], v[176:179], v[200:203], v[98:101]
	v_mfma_f32_16x16x32_bf16 v[94:97], v[184:187], v[200:203], v[94:97]
	v_mfma_f32_16x16x32_bf16 v[82:85], v[176:179], v[208:211], v[82:85]
	v_mfma_f32_16x16x32_bf16 v[78:81], v[184:187], v[208:211], v[78:81]
	v_mfma_f32_16x16x32_bf16 v[70:73], v[176:179], v[216:219], v[70:73]
	v_mfma_f32_16x16x32_bf16 v[66:69], v[184:187], v[216:219], v[66:69]
	s_setprio 0
	s_barrier
; #define PG8_STAGE(bufoff, gbase, voff) do { _Pragma("unroll") for (int _i = 0; _i < 2; ++_i) \
;         __builtin_amdgcn_global_load_lds((const unsigned*)((const char*)(gbase) + (voff)[_i]), (PG8_LAS unsigned*)(lds + (bufoff) + ldsw + _i * 8192), 16, 0, 0); } while (0)
; #define PG8_STAGE_A(bufoff, kbase, h, gv) do { if constexpr (GATHER) { PG8_STAGE(bufoff, kbase, (gv)[h]); } else { PG8_STAGE(bufoff, (kbase) + (h) * hstep, voffA); } } while (0)
; #define PG8_WAIT_V(n) asm volatile("s_waitcnt vmcnt(" #n ")" ::: "memory")
; #define PG8_WAIT_L(n) asm volatile("s_waitcnt lgkmcnt(" #n ")" ::: "memory")
; #define PG8_BAR __builtin_amdgcn_s_barrier()
; #define PG8_SCHED __builtin_amdgcn_sched_barrier(0)
; template <class Epi, class Sched, bool ALIGN_EPI = false, bool SP2 = false, bool FP8 = false, bool GATHER = false>
; __device__ __forceinline__ void gemm_phase(PG8_LAS unsigned char* lds, const Gemm g, const Sched& S, const Epi& E) {
;     ...
;         for (int t = 0; t < nt; t += 2) {
;             const bool last = (t == nt - 2);
;             const char* a1 = cA + (size_t)(t + 1) * kstep;
;             const char* a2 = last ? nA : cA + (size_t)(t + 2) * kstep; const char* b2 = last ? nB : cB + (size_t)(t + 2) * kstep;
;     ...
;             PG8_LDA(At, 1, 1); PG8_STAGE(PG8_SB(1, 0), b3, voffB); PG8_STAGE(PG8_SB(1, 1), b3 + hstep, voffB); PG8_STAGE_A(PG8_SA(1, 0), a3, 0, gsel);
;             PG8_WAIT_V(8); PG8_WAIT_L(0); PG8_BAR; PG8_MMA(1, 0, At, B0); PG8_MMA(1, 1, At, B1); PG8_BAR; PG8_SCHED;
	s_add_i32 s58, s87, s66
	v_lshl_add_u64 v[136:137], v[220:221], 0, s[16:17]
	s_mov_b32 m0, s58
	ds_read_b128 v[188:191], v170 offset:49152
	ds_read_b128 v[192:195], v170 offset:50176
	ds_read_b128 v[196:199], v170 offset:51200
	ds_read_b128 v[200:203], v170 offset:52224
	ds_read_b128 v[204:207], v170 offset:53248
	ds_read_b128 v[208:211], v170 offset:54272
	ds_read_b128 v[212:215], v170 offset:55296
	ds_read_b128 v[216:219], v170 offset:56320
	global_load_lds_dwordx4 v[136:137], off
	s_add_i32 m0, s58, 0x2000
	s_add_u32 s56, s56, 0x40080
	v_lshl_add_u64 v[136:137], v[222:223], 0, s[16:17]
	s_addc_u32 s57, s57, 0
	s_add_i32 s58, s88, s66
	global_load_lds_dwordx4 v[136:137], off
	v_lshl_add_u64 v[136:137], s[56:57], 0, v[148:149]
	s_mov_b32 m0, s58
	s_nop 0
	global_load_lds_dwordx4 v[136:137], off
	v_lshl_add_u64 v[136:137], s[56:57], 0, v[152:153]
	s_add_i32 m0, s58, 0x2000
	s_nop 0
	global_load_lds_dwordx4 v[136:137], off
	v_lshl_add_u64 v[136:137], v[224:225], 0, s[16:17]
	s_mov_b32 m0, s75
	s_nop 0
	global_load_lds_dwordx4 v[136:137], off
	v_lshl_add_u64 v[136:137], v[226:227], 0, s[16:17]
	s_mov_b32 m0, s76
	s_nop 0
	global_load_lds_dwordx4 v[136:137], off
	s_waitcnt vmcnt(8)
	s_waitcnt lgkmcnt(0)
	s_barrier
	s_setprio 1
	s_waitcnt lgkmcnt(0)
	v_mfma_f32_16x16x32_bf16 v[62:65], v[124:127], v[188:191], v[62:65]
	v_mfma_f32_16x16x32_bf16 v[58:61], v[132:135], v[188:191], v[58:61]
	v_mfma_f32_16x16x32_bf16 v[54:57], v[124:127], v[196:199], v[54:57]
	v_mfma_f32_16x16x32_bf16 v[42:45], v[132:135], v[196:199], v[42:45]
	v_mfma_f32_16x16x32_bf16 v[38:41], v[124:127], v[204:207], v[38:41]
	v_mfma_f32_16x16x32_bf16 v[26:29], v[132:135], v[204:207], v[26:29]
	v_mfma_f32_16x16x32_bf16 v[22:25], v[124:127], v[212:215], v[22:25]
	v_mfma_f32_16x16x32_bf16 v[10:13], v[132:135], v[212:215], v[10:13]
	v_mfma_f32_16x16x32_bf16 v[62:65], v[128:131], v[192:195], v[62:65]
	v_mfma_f32_16x16x32_bf16 v[58:61], v[164:167], v[192:195], v[58:61]
	v_mfma_f32_16x16x32_bf16 v[54:57], v[128:131], v[200:203], v[54:57]
	v_mfma_f32_16x16x32_bf16 v[42:45], v[164:167], v[200:203], v[42:45]
	v_mfma_f32_16x16x32_bf16 v[38:41], v[128:131], v[208:211], v[38:41]
	v_mfma_f32_16x16x32_bf16 v[26:29], v[164:167], v[208:211], v[26:29]
	v_mfma_f32_16x16x32_bf16 v[22:25], v[128:131], v[216:219], v[22:25]
	v_mfma_f32_16x16x32_bf16 v[10:13], v[164:167], v[216:219], v[10:13]
	s_setprio 0
	s_setprio 1
	v_mfma_f32_16x16x32_bf16 v[50:53], v[172:175], v[188:191], v[50:53]
	v_mfma_f32_16x16x32_bf16 v[46:49], v[180:183], v[188:191], v[46:49]
	v_mfma_f32_16x16x32_bf16 v[34:37], v[172:175], v[196:199], v[34:37]
	v_mfma_f32_16x16x32_bf16 v[30:33], v[180:183], v[196:199], v[30:33]
	v_mfma_f32_16x16x32_bf16 v[18:21], v[172:175], v[204:207], v[18:21]
	v_mfma_f32_16x16x32_bf16 v[14:17], v[180:183], v[204:207], v[14:17]
	v_mfma_f32_16x16x32_bf16 v[6:9], v[172:175], v[212:215], v[6:9]
	v_mfma_f32_16x16x32_bf16 v[2:5], v[180:183], v[212:215], v[2:5]
	v_mfma_f32_16x16x32_bf16 v[50:53], v[176:179], v[192:195], v[50:53]
	v_mfma_f32_16x16x32_bf16 v[46:49], v[184:187], v[192:195], v[46:49]
	v_mfma_f32_16x16x32_bf16 v[34:37], v[176:179], v[200:203], v[34:37]
	v_mfma_f32_16x16x32_bf16 v[30:33], v[184:187], v[200:203], v[30:33]
	v_mfma_f32_16x16x32_bf16 v[18:21], v[176:179], v[208:211], v[18:21]
	v_mfma_f32_16x16x32_bf16 v[14:17], v[184:187], v[208:211], v[14:17]
	v_mfma_f32_16x16x32_bf16 v[6:9], v[176:179], v[216:219], v[6:9]
	v_mfma_f32_16x16x32_bf16 v[2:5], v[184:187], v[216:219], v[2:5]
	s_setprio 0
	s_add_i32 s86, s86, 2
	s_add_u32 s54, s54, 0x100
	s_addc_u32 s55, s55, 0
	s_add_u32 s53, s53, 0x100
	s_addc_u32 s85, s85, 0
	s_cmp_gt_u32 s86, 13
	s_cbranch_scc1 .Lrot1497_exit
	s_barrier
	s_branch .LBB0_1498
